# MoE2: bias rows loaded at unit start instead of in the epilogue behind vmcnt(0)
# speedup vs baseline: 1.0253x; 1.0029x over previous
.LBB0_2150:
	s_ashr_i32 s13, s12, 31
	s_lshl_b64 s[22:23], s[12:13], 19
	s_add_u32 s24, s6, s22
	s_addc_u32 s25, s7, s23
	s_and_b64 s[22:23], s[54:55], exec
	s_cselect_b32 s13, s25, s57
	s_cselect_b32 s58, s24, s56
	s_ashr_i32 s9, s8, 31
	s_lshl_b64 s[22:23], s[8:9], 22
	s_add_u32 s9, s88, s22
	s_addc_u32 s59, s89, s23
	s_ashr_i32 s5, s4, 31
	s_lshl_b64 s[22:23], s[4:5], 19
	s_add_u32 s22, s9, s22
	s_addc_u32 s23, s59, s23
	s_and_b64 s[62:63], s[54:55], exec
	s_cselect_b32 s5, s23, s61
	s_cselect_b32 s9, s22, s60
	s_add_u32 s56, s56, 0x40080
	s_addc_u32 s57, s57, 0
	s_add_u32 s59, s60, 0x100
	v_mov_b32_e32 v34, 0
	s_addc_u32 s78, s61, 0
	s_mov_b32 s79, -2
	v_mov_b32_e32 v35, v34
	v_mov_b32_e32 v36, v34
	v_mov_b32_e32 v37, v34
	v_mov_b32_e32 v38, v34
	v_mov_b32_e32 v39, v34
	v_mov_b32_e32 v40, v34
	v_mov_b32_e32 v41, v34
	v_mov_b32_e32 v46, v34
	v_mov_b32_e32 v47, v34
	v_mov_b32_e32 v48, v34
	v_mov_b32_e32 v49, v34
	v_mov_b32_e32 v54, v34
	v_mov_b32_e32 v55, v34
	v_mov_b32_e32 v56, v34
	v_mov_b32_e32 v57, v34
	v_mov_b32_e32 v62, v34
	v_mov_b32_e32 v63, v34
	v_mov_b32_e32 v64, v34
	v_mov_b32_e32 v65, v34
	v_mov_b32_e32 v70, v34
	v_mov_b32_e32 v71, v34
	v_mov_b32_e32 v72, v34
	v_mov_b32_e32 v73, v34
	v_mov_b32_e32 v78, v34
	v_mov_b32_e32 v79, v34
	v_mov_b32_e32 v80, v34
	v_mov_b32_e32 v81, v34
	v_mov_b32_e32 v86, v34
	v_mov_b32_e32 v87, v34
	v_mov_b32_e32 v88, v34
	v_mov_b32_e32 v89, v34
	v_mov_b32_e32 v42, v34
	v_mov_b32_e32 v43, v34
	v_mov_b32_e32 v44, v34
	v_mov_b32_e32 v45, v34
	v_mov_b32_e32 v50, v34
	v_mov_b32_e32 v51, v34
	v_mov_b32_e32 v52, v34
	v_mov_b32_e32 v53, v34
	v_mov_b32_e32 v58, v34
	v_mov_b32_e32 v59, v34
	v_mov_b32_e32 v60, v34
	v_mov_b32_e32 v61, v34
	v_mov_b32_e32 v66, v34
	v_mov_b32_e32 v67, v34
	v_mov_b32_e32 v68, v34
	v_mov_b32_e32 v69, v34
	v_mov_b32_e32 v74, v34
	v_mov_b32_e32 v75, v34
	v_mov_b32_e32 v76, v34
	v_mov_b32_e32 v77, v34
	v_mov_b32_e32 v82, v34
	v_mov_b32_e32 v83, v34
	v_mov_b32_e32 v84, v34
	v_mov_b32_e32 v85, v34
	v_mov_b32_e32 v90, v34
	v_mov_b32_e32 v91, v34
	v_mov_b32_e32 v92, v34
	v_mov_b32_e32 v93, v34
	v_mov_b32_e32 v94, v34
	v_mov_b32_e32 v95, v34
	v_mov_b32_e32 v96, v34
	v_mov_b32_e32 v97, v34
	v_mov_b32_e32 v98, v34
	v_mov_b32_e32 v99, v34
	v_mov_b32_e32 v100, v34
	v_mov_b32_e32 v101, v34
	v_mov_b32_e32 v102, v34
	v_mov_b32_e32 v103, v34
	v_mov_b32_e32 v104, v34
	v_mov_b32_e32 v105, v34
	v_mov_b32_e32 v110, v34
	v_mov_b32_e32 v111, v34
	v_mov_b32_e32 v112, v34
	v_mov_b32_e32 v113, v34
	v_mov_b32_e32 v118, v34
	v_mov_b32_e32 v119, v34
	v_mov_b32_e32 v120, v34
	v_mov_b32_e32 v121, v34
	v_mov_b32_e32 v126, v34
	v_mov_b32_e32 v127, v34
	v_mov_b32_e32 v128, v34
	v_mov_b32_e32 v129, v34
	v_mov_b32_e32 v134, v34
	v_mov_b32_e32 v135, v34
	v_mov_b32_e32 v136, v34
	v_mov_b32_e32 v137, v34
	v_mov_b32_e32 v142, v34
	v_mov_b32_e32 v143, v34
	v_mov_b32_e32 v144, v34
	v_mov_b32_e32 v145, v34
	v_mov_b32_e32 v150, v34
	v_mov_b32_e32 v151, v34
	v_mov_b32_e32 v152, v34
	v_mov_b32_e32 v153, v34
	v_mov_b32_e32 v106, v34
	v_mov_b32_e32 v107, v34
	v_mov_b32_e32 v108, v34
	v_mov_b32_e32 v109, v34
	v_mov_b32_e32 v114, v34
	v_mov_b32_e32 v115, v34
	v_mov_b32_e32 v116, v34
	v_mov_b32_e32 v117, v34
	v_mov_b32_e32 v122, v34
	v_mov_b32_e32 v123, v34
	v_mov_b32_e32 v124, v34
	v_mov_b32_e32 v125, v34
	v_mov_b32_e32 v130, v34
	v_mov_b32_e32 v131, v34
	v_mov_b32_e32 v132, v34
	v_mov_b32_e32 v133, v34
	v_mov_b32_e32 v138, v34
	v_mov_b32_e32 v139, v34
	v_mov_b32_e32 v140, v34
	v_mov_b32_e32 v141, v34
	v_mov_b32_e32 v146, v34
	v_mov_b32_e32 v147, v34
	v_mov_b32_e32 v148, v34
	v_mov_b32_e32 v149, v34
	v_mov_b32_e32 v154, v34
	v_mov_b32_e32 v155, v34
	v_mov_b32_e32 v156, v34
	v_mov_b32_e32 v157, v34
	v_mov_b32_e32 v158, v34
	v_mov_b32_e32 v159, v34
	v_mov_b32_e32 v160, v34
	v_mov_b32_e32 v161, v34
	v_lshl_or_b32 v254, s1, 8, v183
	s_mov_b32 s98, s0
	s_ashr_i32 s99, s0, 31
	s_lshl_b64 s[98:99], s[98:99], 13
	s_add_u32 s98, s44, s98
	s_addc_u32 s99, s45, s99
	v_ashrrev_i32_e32 v255, 31, v254
	v_lshl_add_u64 v[254:255], v[254:255], 2, s[98:99]
	global_load_dwordx4 v[238:241], v[254:255], off
	global_load_dwordx4 v[242:245], v[254:255], off offset:16
	global_load_dwordx4 v[246:249], v[254:255], off offset:512
	global_load_dwordx4 v[250:253], v[254:255], off offset:528

.LBB0_2154:
	v_lshl_or_b32 v18, s1, 8, v183
	s_ashr_i32 s1, s0, 31
	s_lshl_b64 s[0:1], s[0:1], 13
	s_add_u32 s0, s44, s0
	s_addc_u32 s1, s45, s1
	v_ashrrev_i32_e32 v19, 31, v18
	v_cndmask_b32_e64 v3, 0, 1, s[20:21]
	v_lshl_add_u64 v[20:21], v[18:19], 2, s[0:1]
	v_mov_b32_e32 v2, 0
	v_cmp_ne_u32_e64 s[0:1], 1, v3
	s_andn2_b64 vcc, exec, s[20:21]
	v_mov_b32_e32 v6, 0
	v_mov_b32_e32 v7, 0
	v_mov_b32_e32 v8, 0
	v_mov_b32_e32 v9, 0
	s_nop 15
	s_nop 15
	s_nop 15
	s_nop 15
	s_cbranch_vccnz .LBB0_2156
	v_mov_b32_e32 v6, v238
	v_mov_b32_e32 v7, v239
	v_mov_b32_e32 v8, v240
	v_mov_b32_e32 v9, v241
.LBB0_2156:
	s_and_b64 vcc, exec, s[0:1]
	v_mov_b32_e32 v3, 0
	v_mov_b32_e32 v4, 0
	v_mov_b32_e32 v5, 0
	s_cbranch_vccnz .LBB0_2158
	v_mov_b32_e32 v2, v242
	v_mov_b32_e32 v3, v243
	v_mov_b32_e32 v4, v244
	v_mov_b32_e32 v5, v245
.LBB0_2158:
	v_mov_b32_e32 v10, 0
	s_and_b64 vcc, exec, s[0:1]
	v_mov_b32_e32 v14, 0
	v_mov_b32_e32 v15, 0
	v_mov_b32_e32 v16, 0
	v_mov_b32_e32 v17, 0
	s_cbranch_vccnz .LBB0_2160
	v_mov_b32_e32 v14, v246
	v_mov_b32_e32 v15, v247
	v_mov_b32_e32 v16, v248
	v_mov_b32_e32 v17, v249
.LBB0_2160:
	s_and_b64 vcc, exec, s[0:1]
	v_mov_b32_e32 v11, 0
	v_mov_b32_e32 v12, 0
	v_mov_b32_e32 v13, 0
	s_cbranch_vccnz .LBB0_2162
	v_mov_b32_e32 v10, v250
	v_mov_b32_e32 v11, v251
	v_mov_b32_e32 v12, v252
	v_mov_b32_e32 v13, v253
.LBB0_2162:
	v_lshl_add_u32 v24, s77, 8, v1
	v_ashrrev_i32_e32 v25, 31, v24
	v_lshlrev_b64 v[20:21], 12, v[24:25]
	v_lshl_add_u64 v[20:21], s[10:11], 0, v[20:21]
	v_lshlrev_b64 v[26:27], 1, v[18:19]
	v_lshl_add_u64 v[18:19], v[20:21], 0, v[26:27]
	v_pk_fma_f32 v[20:21], v[158:159], s[26:27], v[6:7] op_sel_hi:[1,0,1]
	v_pk_fma_f32 v[22:23], v[160:161], s[26:27], v[8:9] op_sel_hi:[1,0,1]
	v_cvt_pk_bf16_f32 v20, v20, v21
	v_pk_fma_f32 v[28:29], v[156:157], s[26:27], v[4:5] op_sel_hi:[1,0,1]
	v_cvt_pk_bf16_f32 v21, v22, v23
	v_pk_fma_f32 v[30:31], v[154:155], s[26:27], v[2:3] op_sel_hi:[1,0,1]
	v_pk_fma_f32 v[32:33], v[138:139], s[26:27], v[2:3] op_sel_hi:[1,0,1]
	v_cvt_pk_bf16_f32 v22, v30, v31
	v_cvt_pk_bf16_f32 v23, v28, v29
	global_store_dwordx4 v[18:19], v[20:23], off
	v_pk_fma_f32 v[28:29], v[144:145], s[26:27], v[12:13] op_sel_hi:[1,0,1]
	v_pk_fma_f32 v[30:31], v[142:143], s[26:27], v[10:11] op_sel_hi:[1,0,1]
	v_pk_fma_f32 v[20:21], v[150:151], s[26:27], v[14:15] op_sel_hi:[1,0,1]
	v_pk_fma_f32 v[22:23], v[152:153], s[26:27], v[16:17] op_sel_hi:[1,0,1]
	v_cvt_pk_bf16_f32 v20, v20, v21
	s_mov_b64 s[0:1], -1
	v_cvt_pk_bf16_f32 v21, v22, v23
	v_cvt_pk_bf16_f32 v22, v30, v31
	v_cvt_pk_bf16_f32 v23, v28, v29
	global_store_dwordx4 v[18:19], v[20:23], off offset:256
	v_pk_fma_f32 v[30:31], v[140:141], s[26:27], v[4:5] op_sel_hi:[1,0,1]
	s_nop 0
	v_or_b32_e32 v20, 16, v24
	v_ashrrev_i32_e32 v21, 31, v20
	v_lshlrev_b64 v[20:21], 12, v[20:21]
	v_lshl_add_u64 v[20:21], s[10:11], 0, v[20:21]
	v_lshl_add_u64 v[28:29], v[20:21], 0, v[26:27]
	v_pk_fma_f32 v[20:21], v[146:147], s[26:27], v[6:7] op_sel_hi:[1,0,1]
	v_pk_fma_f32 v[22:23], v[148:149], s[26:27], v[8:9] op_sel_hi:[1,0,1]
	v_cvt_pk_bf16_f32 v20, v20, v21
	s_nop 0
	v_cvt_pk_bf16_f32 v21, v22, v23
	v_cvt_pk_bf16_f32 v22, v32, v33
	v_cvt_pk_bf16_f32 v23, v30, v31
	global_store_dwordx4 v[28:29], v[20:23], off
	v_pk_fma_f32 v[30:31], v[128:129], s[26:27], v[12:13] op_sel_hi:[1,0,1]
	v_pk_fma_f32 v[32:33], v[126:127], s[26:27], v[10:11] op_sel_hi:[1,0,1]
	v_pk_fma_f32 v[20:21], v[134:135], s[26:27], v[14:15] op_sel_hi:[1,0,1]
	v_pk_fma_f32 v[22:23], v[136:137], s[26:27], v[16:17] op_sel_hi:[1,0,1]
	v_cvt_pk_bf16_f32 v20, v20, v21
	s_nop 0
	v_cvt_pk_bf16_f32 v21, v22, v23
	v_cvt_pk_bf16_f32 v22, v32, v33
	v_cvt_pk_bf16_f32 v23, v30, v31
	global_store_dwordx4 v[28:29], v[20:23], off offset:256
	v_pk_fma_f32 v[30:31], v[124:125], s[26:27], v[4:5] op_sel_hi:[1,0,1]
	v_pk_fma_f32 v[32:33], v[122:123], s[26:27], v[2:3] op_sel_hi:[1,0,1]
	v_or_b32_e32 v20, 32, v24
	v_ashrrev_i32_e32 v21, 31, v20
	v_lshlrev_b64 v[20:21], 12, v[20:21]
	v_lshl_add_u64 v[20:21], s[10:11], 0, v[20:21]
	v_lshl_add_u64 v[28:29], v[20:21], 0, v[26:27]
	v_pk_fma_f32 v[20:21], v[130:131], s[26:27], v[6:7] op_sel_hi:[1,0,1]
	v_pk_fma_f32 v[22:23], v[132:133], s[26:27], v[8:9] op_sel_hi:[1,0,1]
	v_cvt_pk_bf16_f32 v20, v20, v21
	s_nop 0
	v_cvt_pk_bf16_f32 v21, v22, v23
	v_cvt_pk_bf16_f32 v22, v32, v33
	v_cvt_pk_bf16_f32 v23, v30, v31
	global_store_dwordx4 v[28:29], v[20:23], off
	v_pk_fma_f32 v[30:31], v[112:113], s[26:27], v[12:13] op_sel_hi:[1,0,1]
	v_pk_fma_f32 v[32:33], v[110:111], s[26:27], v[10:11] op_sel_hi:[1,0,1]
	v_pk_fma_f32 v[20:21], v[118:119], s[26:27], v[14:15] op_sel_hi:[1,0,1]
	v_pk_fma_f32 v[22:23], v[120:121], s[26:27], v[16:17] op_sel_hi:[1,0,1]
	v_cvt_pk_bf16_f32 v20, v20, v21
	s_nop 0
	v_cvt_pk_bf16_f32 v21, v22, v23
	v_cvt_pk_bf16_f32 v22, v32, v33
	v_cvt_pk_bf16_f32 v23, v30, v31
	global_store_dwordx4 v[28:29], v[20:23], off offset:256
	v_pk_fma_f32 v[28:29], v[106:107], s[26:27], v[2:3] op_sel_hi:[1,0,1]
	s_nop 0
	v_or_b32_e32 v20, 48, v24
	v_ashrrev_i32_e32 v21, 31, v20
	v_lshlrev_b64 v[20:21], 12, v[20:21]
	v_lshl_add_u64 v[20:21], s[10:11], 0, v[20:21]
	v_lshl_add_u64 v[24:25], v[20:21], 0, v[26:27]
	v_pk_fma_f32 v[22:23], v[116:117], s[26:27], v[8:9] op_sel_hi:[1,0,1]
	v_pk_fma_f32 v[20:21], v[114:115], s[26:27], v[6:7] op_sel_hi:[1,0,1]
	v_pk_fma_f32 v[26:27], v[108:109], s[26:27], v[4:5] op_sel_hi:[1,0,1]
	v_cvt_pk_bf16_f32 v20, v20, v21
	v_cvt_pk_bf16_f32 v21, v22, v23
	v_cvt_pk_bf16_f32 v22, v28, v29
	v_pk_fma_f32 v[28:29], v[98:99], s[26:27], v[10:11] op_sel_hi:[1,0,1]
	v_cvt_pk_bf16_f32 v23, v26, v27
	global_store_dwordx4 v[24:25], v[20:23], off
	v_pk_fma_f32 v[26:27], v[100:101], s[26:27], v[12:13] op_sel_hi:[1,0,1]
	s_nop 0
	v_pk_fma_f32 v[22:23], v[104:105], s[26:27], v[16:17] op_sel_hi:[1,0,1]
	v_pk_fma_f32 v[20:21], v[102:103], s[26:27], v[14:15] op_sel_hi:[1,0,1]
	s_nop 0
	v_cvt_pk_bf16_f32 v20, v20, v21
	v_cvt_pk_bf16_f32 v21, v22, v23
	v_cvt_pk_bf16_f32 v22, v28, v29
	v_cvt_pk_bf16_f32 v23, v26, v27
	global_store_dwordx4 v[24:25], v[20:23], off offset:256
	v_pk_fma_f32 v[26:27], v[92:93], s[26:27], v[4:5] op_sel_hi:[1,0,1]
	v_pk_fma_f32 v[28:29], v[90:91], s[26:27], v[2:3] op_sel_hi:[1,0,1]
	v_pk_fma_f32 v[22:23], v[96:97], s[26:27], v[8:9] op_sel_hi:[1,0,1]
	v_pk_fma_f32 v[20:21], v[94:95], s[26:27], v[6:7] op_sel_hi:[1,0,1]
	v_lshl_add_u64 v[24:25], v[18:19], 0, s[36:37]
	v_cvt_pk_bf16_f32 v20, v20, v21
	v_cvt_pk_bf16_f32 v21, v22, v23
	v_cvt_pk_bf16_f32 v22, v28, v29
	v_cvt_pk_bf16_f32 v23, v26, v27
	v_add_co_u32_e32 v26, vcc, s73, v18
	v_pk_fma_f32 v[28:29], v[78:79], s[26:27], v[10:11] op_sel_hi:[1,0,1]
	s_nop 0
	v_addc_co_u32_e32 v27, vcc, 0, v19, vcc
	global_store_dwordx4 v[26:27], v[20:23], off
	v_pk_fma_f32 v[26:27], v[80:81], s[26:27], v[12:13] op_sel_hi:[1,0,1]
	s_nop 0
	v_pk_fma_f32 v[22:23], v[88:89], s[26:27], v[16:17] op_sel_hi:[1,0,1]
	v_pk_fma_f32 v[20:21], v[86:87], s[26:27], v[14:15] op_sel_hi:[1,0,1]
	s_nop 0
	v_cvt_pk_bf16_f32 v20, v20, v21
	v_cvt_pk_bf16_f32 v21, v22, v23
	v_cvt_pk_bf16_f32 v22, v28, v29
	v_cvt_pk_bf16_f32 v23, v26, v27
	global_store_dwordx4 v[24:25], v[20:23], off offset:256
	v_pk_fma_f32 v[26:27], v[76:77], s[26:27], v[4:5] op_sel_hi:[1,0,1]
	v_pk_fma_f32 v[28:29], v[74:75], s[26:27], v[2:3] op_sel_hi:[1,0,1]
	v_pk_fma_f32 v[22:23], v[84:85], s[26:27], v[8:9] op_sel_hi:[1,0,1]
	v_pk_fma_f32 v[20:21], v[82:83], s[26:27], v[6:7] op_sel_hi:[1,0,1]
	v_lshl_add_u64 v[24:25], v[18:19], 0, s[40:41]
	v_cvt_pk_bf16_f32 v20, v20, v21
	v_cvt_pk_bf16_f32 v21, v22, v23
	v_cvt_pk_bf16_f32 v22, v28, v29
	v_cvt_pk_bf16_f32 v23, v26, v27
	v_add_co_u32_e32 v26, vcc, s74, v18
	v_pk_fma_f32 v[28:29], v[62:63], s[26:27], v[10:11] op_sel_hi:[1,0,1]
	s_nop 0
	v_addc_co_u32_e32 v27, vcc, 0, v19, vcc
	global_store_dwordx4 v[26:27], v[20:23], off
	v_pk_fma_f32 v[26:27], v[64:65], s[26:27], v[12:13] op_sel_hi:[1,0,1]
	s_nop 0
	v_pk_fma_f32 v[22:23], v[72:73], s[26:27], v[16:17] op_sel_hi:[1,0,1]
	v_pk_fma_f32 v[20:21], v[70:71], s[26:27], v[14:15] op_sel_hi:[1,0,1]
	s_nop 0
	v_cvt_pk_bf16_f32 v20, v20, v21
	v_cvt_pk_bf16_f32 v21, v22, v23
	v_cvt_pk_bf16_f32 v22, v28, v29
	v_cvt_pk_bf16_f32 v23, v26, v27
	global_store_dwordx4 v[24:25], v[20:23], off offset:256
	v_pk_fma_f32 v[26:27], v[60:61], s[26:27], v[4:5] op_sel_hi:[1,0,1]
	v_pk_fma_f32 v[28:29], v[58:59], s[26:27], v[2:3] op_sel_hi:[1,0,1]
	v_pk_fma_f32 v[22:23], v[68:69], s[26:27], v[8:9] op_sel_hi:[1,0,1]
	v_pk_fma_f32 v[20:21], v[66:67], s[26:27], v[6:7] op_sel_hi:[1,0,1]
	v_lshl_add_u64 v[24:25], v[18:19], 0, s[42:43]
	v_cvt_pk_bf16_f32 v20, v20, v21
	v_cvt_pk_bf16_f32 v21, v22, v23
	v_cvt_pk_bf16_f32 v22, v28, v29
	v_cvt_pk_bf16_f32 v23, v26, v27
	v_add_co_u32_e32 v26, vcc, s75, v18
	v_pk_fma_f32 v[28:29], v[46:47], s[26:27], v[10:11] op_sel_hi:[1,0,1]
	s_nop 0
	v_addc_co_u32_e32 v27, vcc, 0, v19, vcc
	global_store_dwordx4 v[26:27], v[20:23], off
	v_pk_fma_f32 v[26:27], v[48:49], s[26:27], v[12:13] op_sel_hi:[1,0,1]
	v_pk_fma_f32 v[6:7], v[50:51], s[26:27], v[6:7] op_sel_hi:[1,0,1]
	v_pk_fma_f32 v[22:23], v[56:57], s[26:27], v[16:17] op_sel_hi:[1,0,1]
	v_pk_fma_f32 v[20:21], v[54:55], s[26:27], v[14:15] op_sel_hi:[1,0,1]
	v_pk_fma_f32 v[8:9], v[52:53], s[26:27], v[8:9] op_sel_hi:[1,0,1]
	v_cvt_pk_bf16_f32 v20, v20, v21
	v_cvt_pk_bf16_f32 v21, v22, v23
	v_cvt_pk_bf16_f32 v22, v28, v29
	v_cvt_pk_bf16_f32 v23, v26, v27
	global_store_dwordx4 v[24:25], v[20:23], off offset:256
	s_nop 1
	v_pk_fma_f32 v[22:23], v[44:45], s[26:27], v[4:5] op_sel_hi:[1,0,1]
	v_pk_fma_f32 v[4:5], v[42:43], s[26:27], v[2:3] op_sel_hi:[1,0,1]
	v_cvt_pk_bf16_f32 v2, v6, v7
	v_add_co_u32_e32 v6, vcc, s76, v18
	v_cvt_pk_bf16_f32 v3, v8, v9
	v_cvt_pk_bf16_f32 v4, v4, v5
	v_cvt_pk_bf16_f32 v5, v22, v23
	v_lshl_add_u64 v[20:21], v[18:19], 0, s[52:53]
	s_nop 0
	v_addc_co_u32_e32 v7, vcc, 0, v19, vcc
	global_store_dwordx4 v[6:7], v[2:5], off
	s_andn2_b64 vcc, exec, s[54:55]
	v_pk_fma_f32 v[6:7], v[36:37], s[26:27], v[12:13] op_sel_hi:[1,0,1]
	v_pk_fma_f32 v[4:5], v[40:41], s[26:27], v[16:17] op_sel_hi:[1,0,1]
	v_pk_fma_f32 v[2:3], v[38:39], s[26:27], v[14:15] op_sel_hi:[1,0,1]
	v_pk_fma_f32 v[8:9], v[34:35], s[26:27], v[10:11] op_sel_hi:[1,0,1]
	v_cvt_pk_bf16_f32 v2, v2, v3
	v_cvt_pk_bf16_f32 v3, v4, v5
	s_nop 0
	v_cvt_pk_bf16_f32 v4, v8, v9
	v_cvt_pk_bf16_f32 v5, v6, v7
	global_store_dwordx4 v[20:21], v[2:5], off offset:256
	s_cbranch_vccnz .LBB0_2143
	s_andn2_b64 vcc, exec, s[14:15]
	s_cbranch_vccnz .LBB0_2142
	s_barrier
	s_branch .LBB0_2142
